# baseline (speedup 1.0000x reference)
_Z11main_kernelPKDv8_DF16bS1_PKfS3_S3_PKiPKtS3_S3_Pf:
	s_lshl_b32 s14, s2, 5
	s_load_dwordx4 s[4:7], s[0:1], 0x0
	s_load_dwordx2 s[36:37], s[0:1], 0x10
	s_load_dwordx4 s[8:11], s[0:1], 0x28
	s_and_b32 s3, s14, 0xe0
	s_lshr_b32 s33, s2, 3
	s_or_b32 s15, s3, s33
	v_lshrrev_b32_e32 v73, 6, v0
	s_lshl_b32 s34, s15, 3
	v_or_b32_e32 v54, s34, v73
	v_mov_b32_e32 v55, 0
	v_and_b32_e32 v1, 63, v0
	v_lshlrev_b64 v[2:3], 7, v[54:55]
	s_waitcnt lgkmcnt(0)
	v_lshl_add_u64 v[2:3], s[10:11], 0, v[2:3]
	v_lshlrev_b32_e32 v4, 1, v1
	v_mov_b32_e32 v5, v55
	v_lshl_add_u64 v[2:3], v[2:3], 0, v[4:5]
	global_load_ushort v72, v[2:3], off
	v_and_b32_e32 v2, 7, v0
	v_bfe_u32 v74, v0, 4, 2
	v_lshlrev_b32_e32 v2, 4, v2
	s_mov_b32 s13, 0
	s_lshl_b32 s2, s15, 1
	s_lshl_b32 s12, s15, 2
	v_lshl_or_b32 v2, v74, 7, v2
	v_mov_b32_e32 v3, v55
	s_and_b32 s10, s2, 0x3ffffffc
	v_lshl_add_u64 v[58:59], s[4:5], 0, v[2:3]
	s_lshl_b64 s[2:3], s[12:13], 9
	v_lshl_add_u64 v[2:3], v[58:59], 0, s[2:3]
	s_or_b32 s2, s12, 1
	s_mov_b32 s3, s13
	s_lshl_b64 s[2:3], s[2:3], 9
	v_lshl_add_u64 v[4:5], v[58:59], 0, s[2:3]
	s_or_b32 s2, s12, 2
	s_mov_b32 s3, s13
	s_lshl_b64 s[2:3], s[2:3], 9
	global_load_dwordx4 v[22:25], v[2:3], off
	global_load_dwordx4 v[50:53], v[4:5], off
	v_lshl_add_u64 v[2:3], v[58:59], 0, s[2:3]
	s_or_b32 s2, s12, 3
	s_mov_b32 s3, s13
	s_lshl_b64 s[2:3], s[2:3], 9
	v_lshl_add_u64 v[4:5], v[58:59], 0, s[2:3]
	s_and_b32 s2, s14, 0x700
	s_add_i32 s5, s33, 1
	s_lshl_b32 s14, s2, 4
	s_lshl_b32 s2, s5, 8
	s_and_b32 s2, s2, 0x700
	s_add_i32 s38, s33, 2
	s_lshl_b32 s16, s2, 4
	s_lshl_b32 s2, s38, 8
	s_and_b32 s2, s2, 0x700
	s_add_i32 s39, s33, 3
	s_lshl_b32 s18, s2, 4
	s_lshl_b32 s2, s39, 8
	s_and_b32 s44, s15, 0x1fffff80
	v_lshlrev_b32_e32 v75, 3, v73
	s_and_b32 s2, s2, 0x700
	s_add_i32 s40, s33, 4
	global_load_dwordx4 v[60:63], v[2:3], off
	global_load_dwordx4 v[64:67], v[4:5], off
	v_or_b32_e32 v2, s44, v75
	v_mov_b32_e32 v3, v55
	s_lshl_b32 s20, s2, 4
	s_lshl_b32 s2, s40, 8
	v_lshlrev_b64 v[2:3], 12, v[2:3]
	s_and_b32 s2, s2, 0x700
	s_add_i32 s41, s33, 5
	v_lshl_add_u64 v[2:3], s[6:7], 0, v[2:3]
	v_lshlrev_b32_e32 v56, 4, v1
	v_mov_b32_e32 v57, v55
	s_lshl_b32 s22, s2, 4
	s_lshl_b32 s2, s41, 8
	v_lshl_add_u64 v[2:3], v[2:3], 0, v[56:57]
	s_mov_b32 s15, s13
	s_and_b32 s2, s2, 0x700
	s_add_i32 s42, s33, 6
	v_lshl_add_u64 v[4:5], v[2:3], 0, s[14:15]
	s_mov_b32 s17, s13
	s_lshl_b32 s24, s2, 4
	s_lshl_b32 s2, s42, 8
	global_load_dwordx4 v[18:21], v[4:5], off
	global_load_dwordx4 v[26:29], v[4:5], off offset:1024
	global_load_dwordx4 v[30:33], v[4:5], off offset:2048
	global_load_dwordx4 v[34:37], v[4:5], off offset:3072
	v_lshl_add_u64 v[4:5], v[2:3], 0, s[16:17]
	s_mov_b32 s19, s13
	s_and_b32 s2, s2, 0x700
	s_add_i32 s43, s33, 7
	global_load_dwordx4 v[38:41], v[4:5], off
	global_load_dwordx4 v[42:45], v[4:5], off offset:1024
	global_load_dwordx4 v[68:71], v[4:5], off offset:2048
	global_load_dwordx4 v[76:79], v[4:5], off offset:3072
	v_lshl_add_u64 v[4:5], v[2:3], 0, s[18:19]
	s_mov_b32 s21, s13
	s_lshl_b32 s26, s2, 4
	s_lshl_b32 s2, s43, 8
	global_load_dwordx4 v[80:83], v[4:5], off
	global_load_dwordx4 v[84:87], v[4:5], off offset:1024
	global_load_dwordx4 v[88:91], v[4:5], off offset:2048
	global_load_dwordx4 v[92:95], v[4:5], off offset:3072
	v_lshl_add_u64 v[4:5], v[2:3], 0, s[20:21]
	s_mov_b32 s23, s13
	s_and_b32 s2, s2, 0x700
	s_and_b32 s30, s34, 0x7ffffc00
	s_mov_b32 s31, s13
	global_load_dwordx4 v[96:99], v[4:5], off
	global_load_dwordx4 v[100:103], v[4:5], off offset:1024
	global_load_dwordx4 v[104:107], v[4:5], off offset:2048
	global_load_dwordx4 v[108:111], v[4:5], off offset:3072
	v_lshl_add_u64 v[4:5], v[2:3], 0, s[22:23]
	s_mov_b32 s25, s13
	s_lshl_b32 s28, s2, 4
	s_lshl_b64 s[2:3], s[30:31], 2
	global_load_dwordx4 v[112:115], v[4:5], off
	global_load_dwordx4 v[116:119], v[4:5], off offset:1024
	global_load_dwordx4 v[120:123], v[4:5], off offset:2048
	global_load_dwordx4 v[124:127], v[4:5], off offset:3072
	v_lshl_add_u64 v[4:5], v[2:3], 0, s[24:25]
	s_mov_b32 s27, s13
	s_mov_b32 s29, s13
	s_add_u32 s2, s36, s2
	global_load_dwordx4 v[128:131], v[4:5], off
	global_load_dwordx4 v[132:135], v[4:5], off offset:1024
	global_load_dwordx4 v[136:139], v[4:5], off offset:2048
	global_load_dwordx4 v[140:143], v[4:5], off offset:3072
	v_lshl_add_u64 v[4:5], v[2:3], 0, s[26:27]
	v_lshl_add_u64 v[2:3], v[2:3], 0, s[28:29]
	s_addc_u32 s3, s37, s3
	global_load_dwordx4 v[144:147], v[4:5], off
	global_load_dwordx4 v[148:151], v[4:5], off offset:1024
	global_load_dwordx4 v[152:155], v[4:5], off offset:2048
	global_load_dwordx4 v[156:159], v[4:5], off offset:3072
	global_load_dwordx4 v[160:163], v[2:3], off
	global_load_dwordx4 v[164:167], v[2:3], off offset:1024
	global_load_dwordx4 v[168:171], v[2:3], off offset:2048
	global_load_dwordx4 v[172:175], v[2:3], off offset:3072
	global_load_dwordx4 v[14:17], v56, s[2:3]
	global_load_dwordx4 v[10:13], v56, s[2:3] offset:1024
	global_load_dwordx4 v[6:9], v56, s[2:3] offset:2048
	s_nop 0
	global_load_dwordx4 v[2:5], v56, s[2:3] offset:3072
	s_load_dwordx2 s[2:3], s[0:1], 0x40
	s_load_dword s15, s[8:9], s10 offset:0x0
	v_lshlrev_b32_e32 v1, 2, v1
	s_waitcnt lgkmcnt(0)
	s_load_dword s4, s[2:3], 0x0
	s_cmp_lg_u32 s15, 1
	s_cbranch_scc1 .Lmy_generic
	s_load_dwordx2 s[0:1], s[0:1], 0x48
	s_mov_b64 s[2:3], -1
	v_lshlrev_b32_e32 v176, 9, v73
	s_movk_i32 s6, 0x4040
	v_and_b32_e32 v177, 15, v0
	v_mad_u32_u24 v176, v74, s6, v176
	v_lshl_or_b32 v176, v177, 2, v176
	s_lshl_b32 s6, s33, 6
	s_and_b32 s6, s6, 0x1c0
	v_add_u32_e32 v177, s6, v176
	s_lshl_b32 s6, s5, 6
	s_and_b32 s6, s6, 0x1c0
	v_add_u32_e32 v178, s6, v176
	s_lshl_b32 s6, s38, 6
	s_and_b32 s6, s6, 0x1c0
	v_add_u32_e32 v179, s6, v176
	s_lshl_b32 s6, s39, 6
	s_and_b32 s6, s6, 0x1c0
	v_add_u32_e32 v180, s6, v176
	s_lshl_b32 s6, s40, 6
	s_and_b32 s6, s6, 0x1c0
	v_add_u32_e32 v181, s6, v176
	s_lshl_b32 s6, s41, 6
	s_and_b32 s6, s6, 0x1c0
	v_add_u32_e32 v182, s6, v176
	s_lshl_b32 s6, s42, 6
	s_and_b32 s6, s6, 0x1c0
	v_add_u32_e32 v183, s6, v176
	s_lshl_b32 s6, s43, 6
	s_and_b32 s6, s6, 0x1c0
	v_add_u32_e32 v184, s6, v176
	s_waitcnt vmcnt(35)
	v_mfma_f32_16x16x32_bf16 v[18:21], v[22:25], v[18:21], 0
	s_waitcnt vmcnt(34)
	v_mfma_f32_16x16x32_bf16 v[18:21], v[50:53], v[26:29], v[18:21]
	s_waitcnt vmcnt(33)
	v_mfma_f32_16x16x32_bf16 v[18:21], v[60:63], v[30:33], v[18:21]
	s_waitcnt vmcnt(32)
	v_mfma_f32_16x16x32_bf16 v[46:49], v[64:67], v[34:37], v[18:21]
	s_waitcnt vmcnt(31)
	v_mfma_f32_16x16x32_bf16 v[18:21], v[22:25], v[38:41], 0
	s_waitcnt vmcnt(30)
	v_mfma_f32_16x16x32_bf16 v[18:21], v[50:53], v[42:45], v[18:21]
	s_waitcnt vmcnt(29)
	v_mfma_f32_16x16x32_bf16 v[18:21], v[60:63], v[68:71], v[18:21]
	s_waitcnt vmcnt(28)
	v_mfma_f32_16x16x32_bf16 v[42:45], v[64:67], v[76:79], v[18:21]
	ds_write_b32 v177, v46
	ds_write_b32 v177, v47 offset:4112
	ds_write_b32 v177, v48 offset:8224
	ds_write_b32 v177, v49 offset:12336
	s_waitcnt vmcnt(27)
	v_mfma_f32_16x16x32_bf16 v[18:21], v[22:25], v[80:83], 0
	s_waitcnt vmcnt(26)
	v_mfma_f32_16x16x32_bf16 v[18:21], v[50:53], v[84:87], v[18:21]
	s_waitcnt vmcnt(25)
	v_mfma_f32_16x16x32_bf16 v[18:21], v[60:63], v[88:91], v[18:21]
	s_waitcnt vmcnt(24)
	v_mfma_f32_16x16x32_bf16 v[38:41], v[64:67], v[92:95], v[18:21]
	ds_write_b32 v178, v42
	ds_write_b32 v178, v43 offset:4112
	ds_write_b32 v178, v44 offset:8224
	ds_write_b32 v178, v45 offset:12336
	s_waitcnt vmcnt(23)
	v_mfma_f32_16x16x32_bf16 v[18:21], v[22:25], v[96:99], 0
	s_waitcnt vmcnt(22)
	v_mfma_f32_16x16x32_bf16 v[18:21], v[50:53], v[100:103], v[18:21]
	s_waitcnt vmcnt(21)
	v_mfma_f32_16x16x32_bf16 v[18:21], v[60:63], v[104:107], v[18:21]
	s_waitcnt vmcnt(20)
	v_mfma_f32_16x16x32_bf16 v[34:37], v[64:67], v[108:111], v[18:21]
	ds_write_b32 v179, v38
	ds_write_b32 v179, v39 offset:4112
	ds_write_b32 v179, v40 offset:8224
	ds_write_b32 v179, v41 offset:12336
	s_waitcnt vmcnt(19)
	v_mfma_f32_16x16x32_bf16 v[18:21], v[22:25], v[112:115], 0
	s_waitcnt vmcnt(18)
	v_mfma_f32_16x16x32_bf16 v[18:21], v[50:53], v[116:119], v[18:21]
	s_waitcnt vmcnt(17)
	v_mfma_f32_16x16x32_bf16 v[18:21], v[60:63], v[120:123], v[18:21]
	s_waitcnt vmcnt(16)
	v_mfma_f32_16x16x32_bf16 v[30:33], v[64:67], v[124:127], v[18:21]
	ds_write_b32 v180, v34
	ds_write_b32 v180, v35 offset:4112
	ds_write_b32 v180, v36 offset:8224
	ds_write_b32 v180, v37 offset:12336
	s_waitcnt vmcnt(15)
	v_mfma_f32_16x16x32_bf16 v[18:21], v[22:25], v[128:131], 0
	s_waitcnt vmcnt(14)
	v_mfma_f32_16x16x32_bf16 v[18:21], v[50:53], v[132:135], v[18:21]
	s_waitcnt vmcnt(13)
	v_mfma_f32_16x16x32_bf16 v[18:21], v[60:63], v[136:139], v[18:21]
	s_waitcnt vmcnt(12)
	v_mfma_f32_16x16x32_bf16 v[26:29], v[64:67], v[140:143], v[18:21]
	ds_write_b32 v181, v30
	ds_write_b32 v181, v31 offset:4112
	ds_write_b32 v181, v32 offset:8224
	ds_write_b32 v181, v33 offset:12336
	s_waitcnt vmcnt(11)
	v_mfma_f32_16x16x32_bf16 v[18:21], v[22:25], v[144:147], 0
	s_waitcnt vmcnt(7)
	v_mfma_f32_16x16x32_bf16 v[22:25], v[22:25], v[160:163], 0
	v_mfma_f32_16x16x32_bf16 v[18:21], v[50:53], v[148:151], v[18:21]
	s_waitcnt vmcnt(6)
	v_mfma_f32_16x16x32_bf16 v[22:25], v[50:53], v[164:167], v[22:25]
	v_mfma_f32_16x16x32_bf16 v[18:21], v[60:63], v[152:155], v[18:21]
	s_waitcnt vmcnt(5)
	v_mfma_f32_16x16x32_bf16 v[22:25], v[60:63], v[168:171], v[22:25]
	ds_write_b32 v182, v26
	ds_write_b32 v182, v27 offset:4112
	ds_write_b32 v182, v28 offset:8224
	ds_write_b32 v182, v29 offset:12336
	v_mfma_f32_16x16x32_bf16 v[18:21], v[64:67], v[156:159], v[18:21]
	s_waitcnt vmcnt(4)
	v_mfma_f32_16x16x32_bf16 v[22:25], v[64:67], v[172:175], v[22:25]
	s_nop 7
	ds_write_b32 v183, v18
	ds_write_b32 v183, v19 offset:4112
	ds_write_b32 v183, v20 offset:8224
	ds_write_b32 v183, v21 offset:12336
	ds_write_b32 v184, v22
	ds_write_b32 v184, v23 offset:4112
	ds_write_b32 v184, v24 offset:8224
	ds_write_b32 v184, v25 offset:12336
	s_branch .LBB1_4
.Lmy_generic:
	s_waitcnt vmcnt(35)
	v_mfma_f32_16x16x32_bf16 v[18:21], v[22:25], v[18:21], 0
	s_cmp_lt_i32 s15, 3
	s_cselect_b64 s[2:3], -1, 0
	s_mov_b64 s[8:9], -1
	s_waitcnt vmcnt(34)
	v_mfma_f32_16x16x32_bf16 v[18:21], v[50:53], v[26:29], v[18:21]
	s_and_b64 vcc, exec, s[2:3]
	s_waitcnt vmcnt(33)
	v_mfma_f32_16x16x32_bf16 v[18:21], v[60:63], v[30:33], v[18:21]
	s_waitcnt vmcnt(32)
	v_mfma_f32_16x16x32_bf16 v[46:49], v[64:67], v[34:37], v[18:21]
	s_waitcnt vmcnt(31)
	v_mfma_f32_16x16x32_bf16 v[18:21], v[22:25], v[38:41], 0
	s_waitcnt vmcnt(30)
	v_mfma_f32_16x16x32_bf16 v[18:21], v[50:53], v[42:45], v[18:21]
	s_waitcnt vmcnt(29)
	v_mfma_f32_16x16x32_bf16 v[18:21], v[60:63], v[68:71], v[18:21]
	s_waitcnt vmcnt(28)
	v_mfma_f32_16x16x32_bf16 v[42:45], v[64:67], v[76:79], v[18:21]
	s_waitcnt vmcnt(27)
	v_mfma_f32_16x16x32_bf16 v[18:21], v[22:25], v[80:83], 0
	s_waitcnt vmcnt(26)
	v_mfma_f32_16x16x32_bf16 v[18:21], v[50:53], v[84:87], v[18:21]
	s_waitcnt vmcnt(25)
	v_mfma_f32_16x16x32_bf16 v[18:21], v[60:63], v[88:91], v[18:21]
	s_waitcnt vmcnt(24)
	v_mfma_f32_16x16x32_bf16 v[38:41], v[64:67], v[92:95], v[18:21]
	s_waitcnt vmcnt(23)
	v_mfma_f32_16x16x32_bf16 v[18:21], v[22:25], v[96:99], 0
	s_waitcnt vmcnt(22)
	v_mfma_f32_16x16x32_bf16 v[18:21], v[50:53], v[100:103], v[18:21]
	s_waitcnt vmcnt(21)
	v_mfma_f32_16x16x32_bf16 v[18:21], v[60:63], v[104:107], v[18:21]
	s_waitcnt vmcnt(20)
	v_mfma_f32_16x16x32_bf16 v[34:37], v[64:67], v[108:111], v[18:21]
	s_waitcnt vmcnt(19)
	v_mfma_f32_16x16x32_bf16 v[18:21], v[22:25], v[112:115], 0
	s_waitcnt vmcnt(18)
	v_mfma_f32_16x16x32_bf16 v[18:21], v[50:53], v[116:119], v[18:21]
	s_waitcnt vmcnt(17)
	v_mfma_f32_16x16x32_bf16 v[18:21], v[60:63], v[120:123], v[18:21]
	s_waitcnt vmcnt(16)
	v_mfma_f32_16x16x32_bf16 v[30:33], v[64:67], v[124:127], v[18:21]
	s_waitcnt vmcnt(15)
	v_mfma_f32_16x16x32_bf16 v[18:21], v[22:25], v[128:131], 0
	s_waitcnt vmcnt(14)
	v_mfma_f32_16x16x32_bf16 v[18:21], v[50:53], v[132:135], v[18:21]
	s_waitcnt vmcnt(13)
	v_mfma_f32_16x16x32_bf16 v[18:21], v[60:63], v[136:139], v[18:21]
	s_waitcnt vmcnt(12)
	v_mfma_f32_16x16x32_bf16 v[26:29], v[64:67], v[140:143], v[18:21]
	s_waitcnt vmcnt(11)
	v_mfma_f32_16x16x32_bf16 v[18:21], v[22:25], v[144:147], 0
	s_waitcnt vmcnt(7)
	v_mfma_f32_16x16x32_bf16 v[22:25], v[22:25], v[160:163], 0
	v_mfma_f32_16x16x32_bf16 v[18:21], v[50:53], v[148:151], v[18:21]
	s_waitcnt vmcnt(6)
	v_mfma_f32_16x16x32_bf16 v[22:25], v[50:53], v[164:167], v[22:25]
	v_mfma_f32_16x16x32_bf16 v[18:21], v[60:63], v[152:155], v[18:21]
	s_waitcnt vmcnt(5)
	v_mfma_f32_16x16x32_bf16 v[22:25], v[60:63], v[168:171], v[22:25]
	v_mfma_f32_16x16x32_bf16 v[18:21], v[64:67], v[156:159], v[18:21]
	s_waitcnt vmcnt(4)
	v_mfma_f32_16x16x32_bf16 v[22:25], v[64:67], v[172:175], v[22:25]
	s_cbranch_vccz .LBB1_5
	s_load_dwordx2 s[0:1], s[0:1], 0x48
	s_and_b64 vcc, exec, s[8:9]
	s_cbranch_vccz .LBB1_4
	s_cmp_lg_u32 s15, 2
	s_cbranch_scc0 .LBB1_14
